# dn_scan loop: counted vmcnt waits, el load pipelined, always-issue prefetch
# speedup vs baseline: 1.0095x; 1.0095x over previous
.LBB0_739:
	v_and_b32_e32 v182, 63, v158
	s_andn2_b64 vcc, exec, s[4:5]
	s_ashr_i32 s54, s55, 6
	s_cbranch_vccnz .LBB0_752
	v_mov_b32_e32 v6, v182
	v_readlane_b32 s4, v252, 63
	s_waitcnt vmcnt(16)
	v_lshlrev_b32_e32 v130, 4, v6
	v_lshl_add_u32 v30, s54, 12, v130
	v_add_u32_e32 v60, 0x400, v30
	v_ashrrev_i32_e32 v31, 31, v30
	v_readlane_b32 s5, v253, 0
	v_ashrrev_i32_e32 v61, 31, v60
	v_add_u32_e32 v78, 0x800, v30
	v_add_u32_e32 v80, 0xc00, v30
	v_lshl_add_u64 v[2:3], s[4:5], 0, v[30:31]
	v_lshl_add_u64 v[4:5], s[4:5], 0, v[60:61]
	v_ashrrev_i32_e32 v79, 31, v78
	v_ashrrev_i32_e32 v81, 31, v80
	v_ashrrev_i32_e32 v159, 31, v158
	global_load_dwordx4 v[74:77], v[2:3], off
	global_load_dwordx4 v[70:73], v[4:5], off
	v_lshl_add_u64 v[2:3], s[4:5], 0, v[78:79]
	v_lshl_add_u64 v[4:5], s[4:5], 0, v[80:81]
	v_lshlrev_b64 v[82:83], 4, v[158:159]
	s_mov_b64 s[4:5], 0x2000
	v_readlane_b32 s6, v253, 1
	v_lshl_add_u64 v[84:85], v[82:83], 0, s[4:5]
	s_mov_b64 s[4:5], 0x4000
	v_readlane_b32 s7, v253, 2
	v_lshl_add_u64 v[86:87], v[82:83], 0, s[4:5]
	s_mov_b64 s[4:5], 0x6000
	global_load_dwordx4 v[66:69], v[2:3], off
	global_load_dwordx4 v[62:65], v[4:5], off
	s_waitcnt lgkmcnt(0)
	s_barrier
	v_lshl_add_u64 v[2:3], s[6:7], 0, v[82:83]
	v_lshl_add_u64 v[88:89], v[82:83], 0, s[4:5]
	s_mov_b64 s[4:5], 0x8000
	v_lshl_add_u64 v[4:5], s[6:7], 0, v[84:85]
	global_load_dwordx4 v[32:35], v[2:3], off
	global_load_dwordx4 v[36:39], v[4:5], off
	v_lshl_add_u64 v[2:3], s[6:7], 0, v[86:87]
	v_lshl_add_u64 v[90:91], v[82:83], 0, s[4:5]
	s_mov_b64 s[4:5], 0xa000
	v_lshl_add_u64 v[4:5], s[6:7], 0, v[88:89]
	global_load_dwordx4 v[40:43], v[2:3], off
	global_load_dwordx4 v[44:47], v[4:5], off
	v_lshl_add_u64 v[2:3], s[6:7], 0, v[90:91]
	v_lshl_add_u64 v[92:93], v[82:83], 0, s[4:5]
	v_lshl_add_u64 v[4:5], s[6:7], 0, v[92:93]
	global_load_dwordx4 v[48:51], v[2:3], off
	global_load_dwordx4 v[52:55], v[4:5], off
	s_mov_b64 s[4:5], 0xc000
	v_lshl_add_u64 v[142:143], v[82:83], 0, s[4:5]
	v_lshl_add_u64 v[2:3], s[6:7], 0, v[142:143]
	global_load_dwordx4 v[56:59], v[2:3], off
	v_ashrrev_i32_e32 v97, 2, v6
	v_and_b32_e32 v4, 15, v6
	v_readlane_b32 s6, v253, 3
	v_and_b32_e32 v128, -4, v97
	v_readlane_b32 s7, v253, 4
	v_lshlrev_b32_e32 v98, 1, v4
	v_add_u32_e32 v4, 48, v128
	v_sub_u32_e32 v5, 15, v128
	v_or_b32_e32 v9, 1, v128
	v_or_b32_e32 v12, 2, v128
	v_lshl_add_u64 v[2:3], s[6:7], 0, v[82:83]
	v_lshl_add_u64 v[6:7], s[6:7], 0, v[84:85]
	v_lshl_add_u64 v[10:11], s[6:7], 0, v[86:87]
	v_lshl_add_u64 v[14:15], s[6:7], 0, v[88:89]
	v_lshl_add_u64 v[18:19], s[6:7], 0, v[90:91]
	v_lshl_add_u64 v[22:23], s[6:7], 0, v[92:93]
	v_lshl_add_u64 v[26:27], s[6:7], 0, v[142:143]
	v_sub_u32_e32 v8, 63, v128
	v_cndmask_b32_e64 v96, v5, v4, s[38:39]
	v_sub_u32_e32 v4, 63, v9
	v_sub_u32_e32 v5, 63, v12
	v_cndmask_b32_e64 v100, v8, v128, s[38:39]
	v_cndmask_b32_e64 v102, v4, v9, s[38:39]
	v_cndmask_b32_e64 v104, v5, v12, s[38:39]
	global_load_dwordx4 v[2:5], v[2:3], off
	s_nop 0
	global_load_dwordx4 v[6:9], v[6:7], off
	s_nop 0
	global_load_dwordx4 v[10:13], v[10:11], off
	s_nop 0
	global_load_dwordx4 v[14:17], v[14:15], off
	s_nop 0
	global_load_dwordx4 v[18:21], v[18:19], off
	s_nop 0
	global_load_dwordx4 v[22:25], v[22:23], off
	s_nop 0
	global_load_dwordx4 v[26:29], v[26:27], off
	v_lshl_add_u32 v152, v158, 4, 0
	s_lshl_b32 s4, s54, 4
	s_ashr_i32 s5, s4, 31
	s_lshl_b64 s[4:5], s[4:5], 1
	v_readlane_b32 s6, v253, 8
	s_add_u32 s4, s6, s4
	v_readlane_b32 s6, v253, 9
	s_addc_u32 s5, s6, s5
	v_lshl_add_u64 v[94:95], s[4:5], 0, v[98:99]
	v_readlane_b32 s4, v254, 13
	v_readlane_b32 s5, v254, 14
	v_add_u32_e32 v153, 0, v130
	v_readlane_b32 s6, v254, 11
	v_lshl_add_u64 v[130:131], s[4:5], 0, v[82:83]
	v_lshl_add_u64 v[132:133], s[4:5], 0, v[84:85]
	v_lshl_add_u64 v[134:135], s[4:5], 0, v[86:87]
	v_lshl_add_u64 v[136:137], s[4:5], 0, v[88:89]
	s_waitcnt vmcnt(19)
	v_lshl_add_u64 v[138:139], s[4:5], 0, v[90:91]
	s_waitcnt vmcnt(18)
	v_lshl_add_u64 v[140:141], s[4:5], 0, v[92:93]
	v_lshl_add_u64 v[142:143], s[4:5], 0, v[142:143]
	s_waitcnt vmcnt(13)
	ds_write_b128 v152, v[32:35]
	s_waitcnt vmcnt(12)
	ds_write_b128 v152, v[36:39] offset:8192
	s_waitcnt vmcnt(11)
	ds_write_b128 v152, v[40:43] offset:16384
	s_waitcnt vmcnt(10)
	ds_write_b128 v152, v[44:47] offset:24576
	s_waitcnt vmcnt(9)
	ds_write_b128 v152, v[48:51] offset:32768
	s_waitcnt vmcnt(8)
	ds_write_b128 v152, v[52:55] offset:40960
	s_waitcnt vmcnt(7)
	ds_write_b128 v152, v[56:59] offset:49152
	v_or_b32_e32 v32, 3, v97
	v_sub_u32_e32 v33, 63, v32
	v_cndmask_b32_e64 v106, v33, v32, s[38:39]
	v_add_u32_e32 v32, 16, v128
	v_sub_u32_e32 v33, 47, v128
	v_cndmask_b32_e64 v108, v33, v32, s[38:39]
	v_add_u32_e32 v32, 17, v128
	v_sub_u32_e32 v33, 46, v128
	v_cndmask_b32_e64 v110, v33, v32, s[38:39]
	v_add_u32_e32 v32, 18, v128
	v_sub_u32_e32 v33, 45, v128
	v_cndmask_b32_e64 v112, v33, v32, s[38:39]
	v_add_u32_e32 v32, 19, v128
	v_sub_u32_e32 v33, 44, v128
	v_cndmask_b32_e64 v114, v33, v32, s[38:39]
	v_add_u32_e32 v32, 32, v128
	v_sub_u32_e32 v33, 31, v128
	v_cndmask_b32_e64 v116, v33, v32, s[38:39]
	v_add_u32_e32 v32, 33, v128
	v_sub_u32_e32 v33, 30, v128
	v_cndmask_b32_e64 v118, v33, v32, s[38:39]
	v_add_u32_e32 v32, 34, v128
	v_sub_u32_e32 v33, 29, v128
	v_cndmask_b32_e64 v120, v33, v32, s[38:39]
	v_add_u32_e32 v32, 35, v128
	v_sub_u32_e32 v33, 28, v128
	v_cndmask_b32_e64 v122, v33, v32, s[38:39]
	v_add_u32_e32 v32, 49, v128
	v_sub_u32_e32 v33, 14, v128
	v_cndmask_b32_e64 v124, v33, v32, s[38:39]
	v_add_u32_e32 v32, 50, v128
	v_sub_u32_e32 v33, 13, v128
	v_readlane_b32 s4, v254, 15
	s_waitcnt lgkmcnt(0)
	s_barrier
	v_cndmask_b32_e64 v126, v33, v32, s[38:39]
	v_add_u32_e32 v32, 51, v128
	v_sub_u32_e32 v33, 12, v128
	v_readlane_b32 s5, v254, 16
	v_cndmask_b32_e64 v128, v33, v32, s[38:39]
	s_mov_b32 s2, -4
	v_lshl_add_u64 v[144:145], s[4:5], 0, v[30:31]
	v_mov_b32_e32 v30, 0
	v_ashrrev_i32_e32 v101, 31, v100
	v_ashrrev_i32_e32 v103, 31, v102
	v_ashrrev_i32_e32 v105, 31, v104
	v_ashrrev_i32_e32 v107, 31, v106
	v_ashrrev_i32_e32 v109, 31, v108
	v_ashrrev_i32_e32 v111, 31, v110
	v_ashrrev_i32_e32 v113, 31, v112
	v_ashrrev_i32_e32 v115, 31, v114
	v_ashrrev_i32_e32 v117, 31, v116
	v_ashrrev_i32_e32 v119, 31, v118
	v_ashrrev_i32_e32 v121, 31, v120
	v_ashrrev_i32_e32 v123, 31, v122
	v_ashrrev_i32_e32 v97, 31, v96
	v_ashrrev_i32_e32 v125, 31, v124
	v_ashrrev_i32_e32 v127, 31, v126
	v_ashrrev_i32_e32 v129, 31, v128
	v_lshl_add_u64 v[146:147], s[4:5], 0, v[60:61]
	v_lshl_add_u64 v[148:149], s[4:5], 0, v[78:79]
	v_lshl_add_u64 v[150:151], s[4:5], 0, v[80:81]
	s_movk_i32 s10, 0x43
	s_mov_b64 s[4:5], 0
	v_readlane_b32 s7, v254, 12
	v_mov_b32_e32 v31, v30
	v_mov_b32_e32 v32, v30
	v_mov_b32_e32 v33, v30
	v_mov_b32_e32 v34, v30
	v_mov_b32_e32 v35, v30
	v_mov_b32_e32 v36, v30
	v_mov_b32_e32 v37, v30
	v_mov_b32_e32 v38, v30
	v_mov_b32_e32 v39, v30
	v_mov_b32_e32 v40, v30
	v_mov_b32_e32 v41, v30
	v_mov_b32_e32 v50, v30
	v_mov_b32_e32 v51, v30
	v_mov_b32_e32 v52, v30
	v_mov_b32_e32 v53, v30
	v_mov_b32_e32 v42, v30
	v_mov_b32_e32 v43, v30
	v_mov_b32_e32 v44, v30
	v_mov_b32_e32 v45, v30
	v_mov_b32_e32 v46, v30
	v_mov_b32_e32 v47, v30
	v_mov_b32_e32 v48, v30
	v_mov_b32_e32 v49, v30
	v_mov_b32_e32 v54, v30
	v_mov_b32_e32 v55, v30
	v_mov_b32_e32 v56, v30
	v_mov_b32_e32 v57, v30
	v_mov_b32_e32 v58, v30
	v_mov_b32_e32 v59, v30
	v_mov_b32_e32 v60, v30
	v_mov_b32_e32 v61, v30
	global_load_dword v98, v99, s[6:7]
	s_waitcnt vmcnt(0)
	s_branch .LBB0_742
.LBB0_741:
	v_readlane_b32 s8, v253, 44
	s_ashr_i32 s9, s12, 31
	s_mulk_i32 s8, 0x4400
	s_add_u32 s8, s12, s8
	s_addc_u32 s9, s9, 0
	v_lshl_add_u64 v[154:155], s[8:9], 0, v[100:101]
	v_lshlrev_b64 v[154:155], 10, v[154:155]
	v_cvt_pk_bf16_f32 v74, v74, s0
	v_lshl_add_u64 v[154:155], v[94:95], 0, v[154:155]
	global_store_short v[154:155], v74, off
	v_cvt_pk_bf16_f32 v156, v75, s0
	v_lshl_add_u64 v[74:75], s[8:9], 0, v[102:103]
	v_lshlrev_b64 v[74:75], 10, v[74:75]
	v_lshl_add_u64 v[74:75], v[94:95], 0, v[74:75]
	global_store_short v[74:75], v156, off
	v_lshl_add_u64 v[74:75], s[8:9], 0, v[104:105]
	v_lshlrev_b64 v[74:75], 10, v[74:75]
	v_cvt_pk_bf16_f32 v76, v76, s0
	v_lshl_add_u64 v[74:75], v[94:95], 0, v[74:75]
	global_store_short v[74:75], v76, off
	v_lshl_add_u64 v[74:75], s[8:9], 0, v[106:107]
	v_lshlrev_b64 v[74:75], 10, v[74:75]
	v_cvt_pk_bf16_f32 v76, v77, s0
	v_lshl_add_u64 v[74:75], v[94:95], 0, v[74:75]
	global_store_short v[74:75], v76, off
	v_lshl_add_u64 v[74:75], s[8:9], 0, v[108:109]
	v_lshlrev_b64 v[74:75], 10, v[74:75]
	v_cvt_pk_bf16_f32 v70, v70, s0
	v_lshl_add_u64 v[74:75], v[94:95], 0, v[74:75]
	global_store_short v[74:75], v70, off
	v_cvt_pk_bf16_f32 v74, v71, s0
	v_lshl_add_u64 v[70:71], s[8:9], 0, v[110:111]
	v_lshlrev_b64 v[70:71], 10, v[70:71]
	v_lshl_add_u64 v[70:71], v[94:95], 0, v[70:71]
	global_store_short v[70:71], v74, off
	v_lshl_add_u64 v[70:71], s[8:9], 0, v[112:113]
	v_lshlrev_b64 v[70:71], 10, v[70:71]
	v_cvt_pk_bf16_f32 v72, v72, s0
	v_lshl_add_u64 v[70:71], v[94:95], 0, v[70:71]
	global_store_short v[70:71], v72, off
	v_lshl_add_u64 v[70:71], s[8:9], 0, v[114:115]
	v_lshlrev_b64 v[70:71], 10, v[70:71]
	v_cvt_pk_bf16_f32 v72, v73, s0
	v_lshl_add_u64 v[70:71], v[94:95], 0, v[70:71]
	global_store_short v[70:71], v72, off
	v_lshl_add_u64 v[70:71], s[8:9], 0, v[116:117]
	v_lshlrev_b64 v[70:71], 10, v[70:71]
	v_cvt_pk_bf16_f32 v66, v66, s0
	v_lshl_add_u64 v[70:71], v[94:95], 0, v[70:71]
	global_store_short v[70:71], v66, off
	v_cvt_pk_bf16_f32 v70, v67, s0
	v_lshl_add_u64 v[66:67], s[8:9], 0, v[118:119]
	v_lshlrev_b64 v[66:67], 10, v[66:67]
	v_lshl_add_u64 v[66:67], v[94:95], 0, v[66:67]
	global_store_short v[66:67], v70, off
	v_lshl_add_u64 v[66:67], s[8:9], 0, v[120:121]
	v_lshlrev_b64 v[66:67], 10, v[66:67]
	v_cvt_pk_bf16_f32 v68, v68, s0
	v_lshl_add_u64 v[66:67], v[94:95], 0, v[66:67]
	global_store_short v[66:67], v68, off
	v_lshl_add_u64 v[66:67], s[8:9], 0, v[122:123]
	v_lshlrev_b64 v[66:67], 10, v[66:67]
	v_cvt_pk_bf16_f32 v68, v69, s0
	v_lshl_add_u64 v[66:67], v[94:95], 0, v[66:67]
	global_store_short v[66:67], v68, off
	v_lshl_add_u64 v[66:67], s[8:9], 0, v[96:97]
	v_lshlrev_b64 v[66:67], 10, v[66:67]
	v_cvt_pk_bf16_f32 v62, v62, s0
	v_lshl_add_u64 v[66:67], v[94:95], 0, v[66:67]
	global_store_short v[66:67], v62, off
	v_cvt_pk_bf16_f32 v66, v63, s0
	v_lshl_add_u64 v[62:63], s[8:9], 0, v[124:125]
	v_lshlrev_b64 v[62:63], 10, v[62:63]
	v_lshl_add_u64 v[62:63], v[94:95], 0, v[62:63]
	global_store_short v[62:63], v66, off
	v_lshl_add_u64 v[62:63], s[8:9], 0, v[126:127]
	v_lshlrev_b64 v[62:63], 10, v[62:63]
	v_cvt_pk_bf16_f32 v64, v64, s0
	v_lshl_add_u64 v[62:63], v[94:95], 0, v[62:63]
	global_store_short v[62:63], v64, off
	v_lshl_add_u64 v[62:63], s[8:9], 0, v[128:129]
	v_lshlrev_b64 v[62:63], 10, v[62:63]
	s_add_i32 s10, s10, -1
	s_add_i32 s2, s2, 1
	v_cvt_pk_bf16_f32 v64, v65, s0
	v_lshl_add_u64 v[62:63], v[94:95], 0, v[62:63]
	s_add_u32 s4, s4, 0x16000
	global_store_short v[62:63], v64, off
	s_addc_u32 s5, s5, 0
	s_waitcnt lgkmcnt(0)
	s_barrier
	s_add_u32 s6, s6, 4
	s_addc_u32 s7, s7, 0
	s_waitcnt vmcnt(17)
	v_mov_b64_e32 v[62:63], v[90:91]
	v_mov_b64_e32 v[66:67], v[86:87]
	v_mov_b64_e32 v[70:71], v[82:83]
	v_mov_b64_e32 v[74:75], v[78:79]
	s_cmp_eq_u32 s4, 0x5d8000
	v_mov_b64_e32 v[64:65], v[92:93]
	v_mov_b64_e32 v[68:69], v[88:89]
	v_mov_b64_e32 v[72:73], v[84:85]
	v_mov_b64_e32 v[76:77], v[80:81]
	s_cbranch_scc1 .LBB0_752
.LBB0_742:
	s_waitcnt vmcnt(17)
	s_cmp_eq_u32 s4, 0x5c2000
	s_cbranch_scc1 .LBB0_744
	s_bitcmp1_b32 s2, 0
	s_cselect_b32 s11, 0, 0xe000
	v_add_u32_e32 v78, s11, v152
	ds_write_b128 v78, v[2:5]
	ds_write_b128 v78, v[6:9] offset:8192
	ds_write_b128 v78, v[10:13] offset:16384
	ds_write_b128 v78, v[14:17] offset:24576
	ds_write_b128 v78, v[18:21] offset:32768
	ds_write_b128 v78, v[22:25] offset:40960
	ds_write_b128 v78, v[26:29] offset:49152
.LBB0_744:
	s_add_i32 s11, s2, 4
	v_lshl_add_u64 v[2:3], v[130:131], 0, s[4:5]
	v_lshl_add_u64 v[6:7], v[132:133], 0, s[4:5]
	v_lshl_add_u64 v[10:11], v[134:135], 0, s[4:5]
	v_lshl_add_u64 v[14:15], v[136:137], 0, s[4:5]
	v_lshl_add_u64 v[18:19], v[138:139], 0, s[4:5]
	v_lshl_add_u64 v[22:23], v[140:141], 0, s[4:5]
	v_lshl_add_u64 v[26:27], v[142:143], 0, s[4:5]
	v_lshl_add_u64 v[78:79], v[144:145], 0, s[4:5]
	v_lshl_add_u64 v[82:83], v[146:147], 0, s[4:5]
	v_lshl_add_u64 v[86:87], v[148:149], 0, s[4:5]
	v_lshl_add_u64 v[90:91], v[150:151], 0, s[4:5]
	global_load_dwordx4 v[2:5], v[2:3], off
	s_nop 0
	global_load_dwordx4 v[6:9], v[6:7], off
	s_nop 0
	global_load_dwordx4 v[10:13], v[10:11], off
	s_nop 0
	global_load_dwordx4 v[14:17], v[14:15], off
	s_nop 0
	global_load_dwordx4 v[18:21], v[18:19], off
	s_nop 0
	global_load_dwordx4 v[22:25], v[22:23], off
	s_nop 0
	global_load_dwordx4 v[26:29], v[26:27], off
	s_nop 0
	global_load_dwordx4 v[78:81], v[78:79], off
	s_nop 0
	global_load_dwordx4 v[82:85], v[82:83], off
	s_nop 0
	global_load_dwordx4 v[86:89], v[86:87], off
	s_nop 0
	global_load_dwordx4 v[90:93], v[90:91], off
.LBB0_748:
	s_bitcmp1_b32 s11, 0
	s_cselect_b32 s8, 0xe000, 0
	v_add_u32_e32 v159, s8, v153
	ds_read_b128 v[154:157], v159 offset:19456
	ds_read_b128 v[160:163], v159 offset:18432
	ds_read_b128 v[164:167], v159 offset:3072
	ds_read_b128 v[168:171], v159 offset:2048
	ds_read_b128 v[172:175], v159 offset:17408
	ds_read_b128 v[176:179], v159 offset:16384
	ds_read_b128 v[184:187], v159 offset:1024
	ds_read_b128 v[188:191], v159
	v_cvt_pk_bf16_f32 v192, v34, v35
	v_cvt_pk_bf16_f32 v193, v36, v37
	v_cvt_pk_bf16_f32 v194, v30, v31
	v_cvt_pk_bf16_f32 v195, v32, v33
	s_waitcnt lgkmcnt(0)
	s_mov_b64 s[8:9], -1
	s_cmp_gt_u32 s11, 3
	v_mfma_f32_16x16x32_bf16 v[74:77], v[188:191], v[192:195], v[74:77]
	v_cvt_pk_bf16_f32 v188, v38, v39
	v_cvt_pk_bf16_f32 v189, v40, v41
	v_cvt_pk_bf16_f32 v190, v50, v51
	v_mfma_f32_16x16x32_bf16 v[176:179], v[176:179], v[192:195], 0
	v_cvt_pk_bf16_f32 v191, v52, v53
	s_waitcnt vmcnt(27)
	v_pk_mul_f32 v[32:33], v[32:33], v[98:99] op_sel_hi:[1,0]
	v_mfma_f32_16x16x32_bf16 v[74:77], v[184:187], v[188:191], v[74:77]
	v_cvt_pk_bf16_f32 v184, v42, v43
	v_cvt_pk_bf16_f32 v185, v44, v45
	v_cvt_pk_bf16_f32 v186, v46, v47
	v_mfma_f32_16x16x32_bf16 v[172:175], v[172:175], v[188:191], v[176:179]
	v_cvt_pk_bf16_f32 v187, v48, v49
	v_pk_mul_f32 v[30:31], v[30:31], v[98:99] op_sel_hi:[1,0]
	v_pk_mul_f32 v[40:41], v[40:41], v[98:99] op_sel_hi:[1,0]
	v_mfma_f32_16x16x32_bf16 v[74:77], v[168:171], v[184:187], v[74:77]
	v_cvt_pk_bf16_f32 v168, v54, v55
	v_cvt_pk_bf16_f32 v169, v56, v57
	v_cvt_pk_bf16_f32 v170, v58, v59
	v_mfma_f32_16x16x32_bf16 v[160:163], v[160:163], v[184:187], v[172:175]
	v_cvt_pk_bf16_f32 v171, v60, v61
	v_pk_mul_f32 v[38:39], v[38:39], v[98:99] op_sel_hi:[1,0]
	v_pk_mul_f32 v[52:53], v[52:53], v[98:99] op_sel_hi:[1,0]
	v_mfma_f32_16x16x32_bf16 v[74:77], v[164:167], v[168:171], v[74:77]
	v_mul_f32_e64 v50, v50, v98
	v_mul_f32_e64 v51, v51, v98
	v_pk_mul_f32 v[44:45], v[44:45], v[98:99] op_sel_hi:[1,0]
	v_pk_mul_f32 v[42:43], v[42:43], v[98:99] op_sel_hi:[1,0]
	v_mfma_f32_16x16x32_bf16 v[154:157], v[154:157], v[168:171], v[160:163]
	s_nop 2
	ds_read_b128 v[160:163], v159 offset:23552
	ds_read_b128 v[164:167], v159 offset:22528
	ds_read_b128 v[172:175], v159 offset:7168
	ds_read_b128 v[176:179], v159 offset:6144
	ds_read_b128 v[202:205], v159 offset:21504
	ds_read_b128 v[206:209], v159 offset:20480
	ds_read_b128 v[210:213], v159 offset:5120
	ds_read_b128 v[214:217], v159 offset:4096
	s_waitcnt lgkmcnt(0)
	s_nop 0
	v_mfma_f32_16x16x32_bf16 v[70:73], v[214:217], v[192:195], v[70:73]
	v_mul_f32_e64 v48, v48, v98
	v_mul_f32_e64 v49, v49, v98
	v_pk_mul_f32 v[46:47], v[46:47], v[98:99] op_sel_hi:[1,0]
	v_pk_mul_f32 v[56:57], v[56:57], v[98:99] op_sel_hi:[1,0]
	v_mfma_f32_16x16x32_bf16 v[206:209], v[206:209], v[192:195], 0
	v_mul_f32_e64 v54, v54, v98
	v_mul_f32_e64 v55, v55, v98
	v_pk_mul_f32 v[60:61], v[60:61], v[98:99] op_sel_hi:[1,0]
	v_pk_mul_f32 v[58:59], v[58:59], v[98:99] op_sel_hi:[1,0]
	v_mfma_f32_16x16x32_bf16 v[70:73], v[210:213], v[188:191], v[70:73]
	v_mul_f32_e64 v36, v36, v98
	v_mul_f32_e64 v37, v37, v98
	v_pk_mul_f32 v[34:35], v[34:35], v[98:99] op_sel_hi:[1,0]
	global_load_dword v98, v99, s[6:7] offset:4
	v_mfma_f32_16x16x32_bf16 v[202:205], v[202:205], v[188:191], v[206:209]
	v_mfma_f32_16x16x32_bf16 v[70:73], v[176:179], v[184:187], v[70:73]
	v_mfma_f32_16x16x32_bf16 v[164:167], v[164:167], v[184:187], v[202:205]
	v_mfma_f32_16x16x32_bf16 v[70:73], v[172:175], v[168:171], v[70:73]
	v_mfma_f32_16x16x32_bf16 v[160:163], v[160:163], v[168:171], v[164:167]
	s_nop 5
	ds_read_b128 v[164:167], v159 offset:27648
	ds_read_b128 v[172:175], v159 offset:26624
	ds_read_b128 v[176:179], v159 offset:11264
	ds_read_b128 v[202:205], v159 offset:10240
	ds_read_b128 v[206:209], v159 offset:25600
	ds_read_b128 v[210:213], v159 offset:24576
	ds_read_b128 v[214:217], v159 offset:9216
	ds_read_b128 v[238:241], v159 offset:8192
	s_waitcnt lgkmcnt(0)
	s_nop 0
	v_mfma_f32_16x16x32_bf16 v[66:69], v[238:241], v[192:195], v[66:69]
	v_mfma_f32_16x16x32_bf16 v[210:213], v[210:213], v[192:195], 0
	v_mfma_f32_16x16x32_bf16 v[66:69], v[214:217], v[188:191], v[66:69]
	v_mfma_f32_16x16x32_bf16 v[206:209], v[206:209], v[188:191], v[210:213]
	v_mfma_f32_16x16x32_bf16 v[66:69], v[202:205], v[184:187], v[66:69]
	v_mfma_f32_16x16x32_bf16 v[172:175], v[172:175], v[184:187], v[206:209]
	v_mfma_f32_16x16x32_bf16 v[66:69], v[176:179], v[168:171], v[66:69]
	v_mfma_f32_16x16x32_bf16 v[164:167], v[164:167], v[168:171], v[172:175]
	s_nop 5
	ds_read_b128 v[172:175], v159 offset:31744
	ds_read_b128 v[176:179], v159 offset:30720
	ds_read_b128 v[202:205], v159 offset:15360
	ds_read_b128 v[206:209], v159 offset:14336
	ds_read_b128 v[210:213], v159 offset:29696
	ds_read_b128 v[214:217], v159 offset:28672
	ds_read_b128 v[238:241], v159 offset:13312
	ds_read_b128 v[242:245], v159 offset:12288
	s_waitcnt lgkmcnt(0)
	s_nop 0
	v_mfma_f32_16x16x32_bf16 v[62:65], v[242:245], v[192:195], v[62:65]
	v_mfma_f32_16x16x32_bf16 v[192:195], v[214:217], v[192:195], 0
	v_mfma_f32_16x16x32_bf16 v[62:65], v[238:241], v[188:191], v[62:65]
	v_cvt_pk_bf16_f32 v238, v66, v67
	v_cvt_pk_bf16_f32 v239, v68, v69
	v_mfma_f32_16x16x32_bf16 v[188:191], v[210:213], v[188:191], v[192:195]
	v_mfma_f32_16x16x32_bf16 v[62:65], v[206:209], v[184:187], v[62:65]
	v_mfma_f32_16x16x32_bf16 v[176:179], v[176:179], v[184:187], v[188:191]
	v_mfma_f32_16x16x32_bf16 v[62:65], v[202:205], v[168:171], v[62:65]
	v_mfma_f32_16x16x32_bf16 v[168:171], v[172:175], v[168:171], v[176:179]
	s_nop 5
	ds_read_b128 v[176:179], v159 offset:48128
	ds_read_b128 v[184:187], v159 offset:47104
	ds_read_b128 v[188:191], v159 offset:46080
	ds_read_b128 v[192:195], v159 offset:45056
	ds_read_b128 v[202:205], v159 offset:44032
	ds_read_b128 v[206:209], v159 offset:43008
	ds_read_b128 v[210:213], v159 offset:41984
	ds_read_b128 v[214:217], v159 offset:40960
	v_cvt_pk_bf16_f32 v172, v74, v75
	v_cvt_pk_bf16_f32 v173, v76, v77
	v_cvt_pk_bf16_f32 v174, v70, v71
	v_cvt_pk_bf16_f32 v175, v72, v73
	s_waitcnt lgkmcnt(0)
	v_cvt_pk_bf16_f32 v240, v62, v63
	v_cvt_pk_bf16_f32 v241, v64, v65
	v_mfma_f32_16x16x32_bf16 v[30:33], v[206:209], v[172:175], v[30:33]
	v_mfma_f32_16x16x32_bf16 v[38:41], v[192:195], v[172:175], v[38:41]
	v_mfma_f32_16x16x32_bf16 v[30:33], v[202:205], v[238:241], v[30:33]
	v_mfma_f32_16x16x32_bf16 v[38:41], v[188:191], v[238:241], v[38:41]
	v_mfma_f32_16x16x32_bf16 v[50:53], v[184:187], v[172:175], v[50:53]
	ds_read_b128 v[62:65], v159 offset:56320
	ds_read_b128 v[66:69], v159 offset:55296
	ds_read_b128 v[70:73], v159 offset:54272
	ds_read_b128 v[74:77], v159 offset:53248
	ds_read_b128 v[184:187], v159 offset:52224
	ds_read_b128 v[188:191], v159 offset:51200
	ds_read_b128 v[192:195], v159 offset:50176
	ds_read_b128 v[202:205], v159 offset:49152
	s_waitcnt lgkmcnt(0)
	s_nop 0
	v_mfma_f32_16x16x32_bf16 v[42:45], v[202:205], v[172:175], v[42:45]
	v_mfma_f32_16x16x32_bf16 v[46:49], v[188:191], v[172:175], v[46:49]
	v_mfma_f32_16x16x32_bf16 v[54:57], v[74:77], v[172:175], v[54:57]
	v_mfma_f32_16x16x32_bf16 v[58:61], v[66:69], v[172:175], v[58:61]
	v_mfma_f32_16x16x32_bf16 v[50:53], v[176:179], v[238:241], v[50:53]
	v_mfma_f32_16x16x32_bf16 v[42:45], v[192:195], v[238:241], v[42:45]
	v_mfma_f32_16x16x32_bf16 v[46:49], v[184:187], v[238:241], v[46:49]
	v_mfma_f32_16x16x32_bf16 v[54:57], v[70:73], v[238:241], v[54:57]
	v_mfma_f32_16x16x32_bf16 v[58:61], v[62:65], v[238:241], v[58:61]
	ds_read_b128 v[62:65], v159 offset:39936
	ds_read_b128 v[176:179], v159 offset:38912
	ds_read_b128 v[66:69], v159 offset:37888
	ds_read_b128 v[184:187], v159 offset:36864
	ds_read_b128 v[70:73], v159 offset:35840
	ds_read_b128 v[188:191], v159 offset:34816
	ds_read_b128 v[74:77], v159 offset:33792
	ds_read_b128 v[192:195], v159 offset:32768
	s_waitcnt lgkmcnt(0)
	s_nop 0
	v_mfma_f32_16x16x32_bf16 v[154:157], v[192:195], v[172:175], v[154:157]
	v_mfma_f32_16x16x32_bf16 v[74:77], v[74:77], v[238:241], v[154:157]
	v_mfma_f32_16x16x32_bf16 v[154:157], v[188:191], v[172:175], v[160:163]
	v_mfma_f32_16x16x32_bf16 v[70:73], v[70:73], v[238:241], v[154:157]
	v_mfma_f32_16x16x32_bf16 v[154:157], v[184:187], v[172:175], v[164:167]
	v_mfma_f32_16x16x32_bf16 v[34:37], v[214:217], v[172:175], v[34:37]
	v_mfma_f32_16x16x32_bf16 v[66:69], v[66:69], v[238:241], v[154:157]
	v_mfma_f32_16x16x32_bf16 v[154:157], v[176:179], v[172:175], v[168:171]
	v_mfma_f32_16x16x32_bf16 v[34:37], v[210:213], v[238:241], v[34:37]
	v_mfma_f32_16x16x32_bf16 v[62:65], v[62:65], v[238:241], v[154:157]
	s_cbranch_scc0 .LBB0_750
	s_and_b64 s[8:9], s[38:39], exec
	s_cselect_b32 s8, s2, s10
	s_lshl_b32 s8, s8, 6
	v_readlane_b32 s9, v253, 5
	s_add_i32 s12, s8, s9
	s_mov_b64 s[8:9], 0

.LBB0_752:
	s_waitcnt vmcnt(0)
	v_readlane_b32 s6, v253, 10
	v_readlane_b32 s7, v253, 11
	v_lshlrev_b32_e32 v2, 2, v182
	v_lshrrev_b32_e32 v3, 3, v182
	v_lshrrev_b32_e32 v153, 1, v182
	v_lshlrev_b32_e32 v4, 5, v182
	s_mov_b64 s[4:5], -1
	s_andn2_b64 vcc, exec, s[6:7]
	v_cmp_eq_u32_e64 s[40:41], 0, v182
	v_and_b32_e32 v152, 28, v2
	v_lshlrev_b32_e32 v154, 13, v3
	v_mul_u32_u24_e32 v159, 0x84, v3
	v_and_b32_e32 v156, 32, v4
	v_lshlrev_b32_e32 v183, 2, v153
	s_cbranch_vccnz .LBB0_836
	v_readlane_b32 s4, v255, 5
	s_lshl_b32 s2, s54, 14
	v_readlane_b32 s5, v255, 6
	s_lshl_b32 s68, s4, 6
	s_add_i32 s8, s2, 0
	s_lshl_b32 s2, s4, 5
	s_lshl_b64 s[4:5], s[68:69], 2
	v_readlane_b32 s6, v253, 12
	v_lshlrev_b32_e32 v2, 2, v152
	s_add_u32 s6, s6, s4
	v_readlane_b32 s7, v253, 13
	v_add3_u32 v80, s8, v2, v159
	v_mul_u32_u24_e32 v2, 0x84, v156
	s_addc_u32 s7, s7, s5
	v_mov_b32_e32 v155, v99
	v_or_b32_e32 v66, 0x10000, v154
	v_mov_b32_e32 v67, v99
	v_or_b32_e32 v68, 0x20000, v154
	v_mov_b32_e32 v69, v99
	v_or_b32_e32 v70, 0x30000, v154
	v_mov_b32_e32 v71, v99
	v_or_b32_e32 v72, 0x40000, v154
	v_mov_b32_e32 v73, v99
	v_or_b32_e32 v74, 0x50000, v154
	v_mov_b32_e32 v75, v99
	v_or_b32_e32 v76, 0x60000, v154
	v_mov_b32_e32 v77, v99
	v_or_b32_e32 v78, 0x70000, v154
	v_mov_b32_e32 v79, v99
	v_add3_u32 v81, s8, v2, v183
	v_mov_b32_e32 v157, v99
	s_barrier
	s_branch .LBB0_756
